# baseline (speedup 1.0000x reference)
.Lk1_nbx7:
.Lk1_nb_done:
	s_lshl_b32 s32, s24, 6
	s_add_u32 s40, s12, s32
	s_addc_u32 s41, s13, 0
	s_lshl_b32 s32, s24, 4
	s_add_u32 s42, s14, s32
	s_addc_u32 s43, s15, 0
	v_lshlrev_b32_e32 v47, 3, v1
	v_lshlrev_b32_e32 v48, 1, v1
	s_mov_b64 exec, 0xff
	global_store_dwordx2 v47, v[44:45], s[40:41]
	global_store_short v48, v46, s[42:43]
	s_mov_b64 exec, -1
	s_load_dwordx4 s[8:11], s[0:1], 0x18
	s_load_dwordx2 s[12:13], s[0:1], 0x28
	s_load_dwordx4 s[16:19], s[0:1], 0x40
	s_mov_b32 s40, 0x652b82fe
	s_mov_b32 s41, 0x3ff71547
	s_mov_b32 s42, 0xfee00000
	s_mov_b32 s43, 0xbfe62e42
	s_mov_b32 s44, 0x35793c76
	s_mov_b32 s45, 0xbdea39ef
	s_mov_b32 s46, 0xb7789f5c
	s_mov_b32 s47, 0x3e927e4f
	s_mov_b32 s48, 0xa556c734
	s_mov_b32 s49, 0x3ec71de3
	s_mov_b32 s50, 0x1a01a01a
	s_mov_b32 s51, 0x3efa01a0
	s_mov_b32 s52, 0x1a01a01a
	s_mov_b32 s53, 0x3f2a01a0
	s_mov_b32 s54, 0x16c16c17
	s_mov_b32 s55, 0x3f56c16c
	s_mov_b32 s56, 0x11111111
	s_mov_b32 s57, 0x3f811111
	s_mov_b32 s58, 0x55555555
	s_mov_b32 s59, 0x3fa55555
	s_mov_b32 s60, 0x55555555
	s_mov_b32 s61, 0x3fc55555
	v_mov_b32_e32 v44, 0x67f544e4
	v_mov_b32_e32 v45, 0x3e5ae645
	s_mov_b32 s62, 0xfefa39ef
	s_mov_b32 s63, 0x3fe62e42
	s_waitcnt vmcnt(4)
	v_readlane_b32 s64, v16, 0
	v_readlane_b32 s65, v17, 0
	v_readlane_b32 s66, v18, 0
	v_readlane_b32 s67, v19, 0
	s_cmp_eq_u32 s35, 1
	s_cselect_b32 s64, s65, s64
	s_cmp_eq_u32 s35, 2
	s_cselect_b32 s64, s66, s64
	s_cmp_eq_u32 s35, 3
	s_cselect_b32 s36, s67, s64
	s_cmp_le_u32 0, s35
	s_cselect_b64 s[32:33], 1, 0
	v_cndmask_b32_e64 v16, v16, v15, s[32:33]
	s_cmp_le_u32 1, s35
	s_cselect_b64 s[32:33], 1, 0
	v_cndmask_b32_e64 v17, v17, v15, s[32:33]
	s_cmp_le_u32 2, s35
	s_cselect_b64 s[32:33], 1, 0
	v_cndmask_b32_e64 v18, v18, v15, s[32:33]
	s_cmp_le_u32 3, s35
	s_cselect_b64 s[32:33], 1, 0
	v_cndmask_b32_e64 v19, v19, v15, s[32:33]
	v_max3_f32 v52, v16, v17, v18
	v_max3_f32 v53, v19, v20, v21
	v_max3_f32 v52, v52, v22, v23
	v_max3_f32 v53, v53, v24, v25
	v_max3_f32 v52, v52, v26, v27
	v_max3_f32 v52, v52, v28, v29
	v_max3_f32 v53, v53, v30, v31
	v_max3_f32 v52, v52, v32, v33
	v_max3_f32 v53, v53, v34, v35
	s_waitcnt vmcnt(2)
	s_cmp_lt_u32 s35, 1
	s_cselect_b64 s[32:33], 0x10000, 0
	v_cndmask_b32_e64 v41, v41, v15, s[32:33]
	s_cmp_lt_u32 s35, 2
	s_cselect_b64 s[32:33], 0x10000, 0
	v_cndmask_b32_e64 v42, v42, v15, s[32:33]
	s_cmp_lt_u32 s35, 3
	s_cselect_b64 s[32:33], 0x10000, 0
	v_cndmask_b32_e64 v43, v43, v15, s[32:33]
	v_max3_f32 v52, v52, v36, v37
	v_max3_f32 v53, v53, v38, v39
	v_max3_f32 v52, v52, v40, v41
	v_max3_f32 v53, v53, v42, v43
	v_max_f32_e32 v52, v52, v53
	s_nop 1
	v_max_f32_dpp v52, v52, v52 quad_perm:[1,0,3,2] row_mask:0xf bank_mask:0xf
	s_nop 1
	v_max_f32_dpp v52, v52, v52 quad_perm:[2,3,0,1] row_mask:0xf bank_mask:0xf
	s_nop 1
	v_max_f32_dpp v52, v52, v52 row_half_mirror row_mask:0xf bank_mask:0xf
	s_nop 1
	v_max_f32_dpp v52, v52, v52 row_mirror row_mask:0xf bank_mask:0xf
	s_nop 1
	v_max_f32_dpp v52, v52, v52 row_bcast:15 row_mask:0xa bank_mask:0xf
	s_nop 1
	v_max_f32_dpp v52, v52, v52 row_bcast:31 row_mask:0xc bank_mask:0xf
	s_nop 1
	v_readlane_b32 s28, v52, 63
	v_mov_b32_e32 v53, s36
	v_mov_b32_e32 v56, 0x3fb8aa3b
	v_mov_b32_e32 v57, 0x3fb8aa3b
	v_max_f32_e32 v53, s28, v53
	v_mul_f32_e32 v58, 0xbfb8aa3b, v53
	v_mov_b32_e32 v6, 0
	v_mov_b32_e32 v7, 0
	v_mov_b32_e32 v59, v58
	v_pk_fma_f32 v[60:61], v[16:17], v[56:57], v[58:59]
	v_pk_fma_f32 v[62:63], v[18:19], v[56:57], v[58:59]
	v_exp_f32_e32 v60, v60
	v_exp_f32_e32 v61, v61
	v_exp_f32_e32 v62, v62
	v_exp_f32_e32 v63, v63
	s_nop 0
	v_pk_add_f32 v[60:61], v[60:61], v[62:63]
	s_nop 0
	v_add_f32_e32 v60, v60, v61
	v_cvt_f64_f32_e32 v[4:5], v60
	v_add_f64 v[6:7], v[6:7], v[4:5]
	v_pk_fma_f32 v[60:61], v[20:21], v[56:57], v[58:59]
	v_pk_fma_f32 v[62:63], v[22:23], v[56:57], v[58:59]
	v_exp_f32_e32 v60, v60
	v_exp_f32_e32 v61, v61
	v_exp_f32_e32 v62, v62
	v_exp_f32_e32 v63, v63
	s_nop 0
	v_pk_add_f32 v[60:61], v[60:61], v[62:63]
	s_nop 0
	v_add_f32_e32 v60, v60, v61
	v_cvt_f64_f32_e32 v[4:5], v60
	v_add_f64 v[6:7], v[6:7], v[4:5]
	v_pk_fma_f32 v[60:61], v[24:25], v[56:57], v[58:59]
	v_pk_fma_f32 v[62:63], v[26:27], v[56:57], v[58:59]
	v_exp_f32_e32 v60, v60
	v_exp_f32_e32 v61, v61
	v_exp_f32_e32 v62, v62
	v_exp_f32_e32 v63, v63
	s_nop 0
	v_pk_add_f32 v[60:61], v[60:61], v[62:63]
	s_nop 0
	v_add_f32_e32 v60, v60, v61
	v_cvt_f64_f32_e32 v[4:5], v60
	v_add_f64 v[6:7], v[6:7], v[4:5]
	v_pk_fma_f32 v[60:61], v[28:29], v[56:57], v[58:59]
	v_pk_fma_f32 v[62:63], v[30:31], v[56:57], v[58:59]
	v_exp_f32_e32 v60, v60
	v_exp_f32_e32 v61, v61
	v_exp_f32_e32 v62, v62
	v_exp_f32_e32 v63, v63
	s_nop 0
	v_pk_add_f32 v[60:61], v[60:61], v[62:63]
	s_nop 0
	v_add_f32_e32 v60, v60, v61
	v_cvt_f64_f32_e32 v[4:5], v60
	v_add_f64 v[6:7], v[6:7], v[4:5]
	v_pk_fma_f32 v[60:61], v[32:33], v[56:57], v[58:59]
	v_pk_fma_f32 v[62:63], v[34:35], v[56:57], v[58:59]
	v_exp_f32_e32 v60, v60
	v_exp_f32_e32 v61, v61
	v_exp_f32_e32 v62, v62
	v_exp_f32_e32 v63, v63
	s_nop 0
	v_pk_add_f32 v[60:61], v[60:61], v[62:63]
	s_nop 0
	v_add_f32_e32 v60, v60, v61
	v_cvt_f64_f32_e32 v[4:5], v60
	v_add_f64 v[6:7], v[6:7], v[4:5]
	v_pk_fma_f32 v[60:61], v[36:37], v[56:57], v[58:59]
	v_pk_fma_f32 v[62:63], v[38:39], v[56:57], v[58:59]
	v_exp_f32_e32 v60, v60
	v_exp_f32_e32 v61, v61
	v_exp_f32_e32 v62, v62
	v_exp_f32_e32 v63, v63
	s_nop 0
	v_pk_add_f32 v[60:61], v[60:61], v[62:63]
	s_nop 0
	v_add_f32_e32 v60, v60, v61
	v_cvt_f64_f32_e32 v[4:5], v60
	v_add_f64 v[6:7], v[6:7], v[4:5]
	v_pk_fma_f32 v[60:61], v[40:41], v[56:57], v[58:59]
	v_pk_fma_f32 v[62:63], v[42:43], v[56:57], v[58:59]
	v_exp_f32_e32 v60, v60
	v_exp_f32_e32 v61, v61
	v_exp_f32_e32 v62, v62
	v_exp_f32_e32 v63, v63
	s_nop 0
	v_pk_add_f32 v[60:61], v[60:61], v[62:63]
	s_nop 0
	v_add_f32_e32 v60, v60, v61
	v_cvt_f64_f32_e32 v[4:5], v60
	v_add_f64 v[6:7], v[6:7], v[4:5]
	v_mov_b32_e32 v60, s36
	v_fmamk_f32 v60, v60, 0x3fb8aa3b, v58
	v_exp_f32_e32 v60, v60
	s_nop 1
	v_mov_b32_dpp v4, v6 quad_perm:[1,0,3,2] row_mask:0xf bank_mask:0xf
	v_mov_b32_dpp v5, v7 quad_perm:[1,0,3,2] row_mask:0xf bank_mask:0xf
	v_add_f64 v[6:7], v[6:7], v[4:5]
	s_nop 1
	v_mov_b32_dpp v4, v6 quad_perm:[2,3,0,1] row_mask:0xf bank_mask:0xf
	v_mov_b32_dpp v5, v7 quad_perm:[2,3,0,1] row_mask:0xf bank_mask:0xf
	v_add_f64 v[6:7], v[6:7], v[4:5]
	s_nop 1
	v_mov_b32_dpp v4, v6 row_half_mirror row_mask:0xf bank_mask:0xf
	v_mov_b32_dpp v5, v7 row_half_mirror row_mask:0xf bank_mask:0xf
	v_add_f64 v[6:7], v[6:7], v[4:5]
	s_nop 1
	v_mov_b32_dpp v4, v6 row_mirror row_mask:0xf bank_mask:0xf
	v_mov_b32_dpp v5, v7 row_mirror row_mask:0xf bank_mask:0xf
	v_add_f64 v[6:7], v[6:7], v[4:5]
	v_cvt_f64_f32_e32 v[8:9], v60
	v_readlane_b32 s64, v6, 15
	v_readlane_b32 s65, v7, 15
	v_readlane_b32 s66, v6, 31
	v_readlane_b32 s67, v7, 31
	v_readlane_b32 s68, v6, 47
	v_readlane_b32 s69, v7, 47
	v_readlane_b32 s70, v6, 63
	v_readlane_b32 s71, v7, 63
	v_add_f64 v[6:7], s[64:65], 0
	v_add_f64 v[6:7], v[6:7], s[66:67]
	v_add_f64 v[6:7], v[6:7], s[68:69]
	v_add_f64 v[6:7], v[6:7], s[70:71]
	v_add_f64 v[6:7], v[6:7], v[8:9]
	s_mov_b32 s29, 1
	s_mov_b32 s31, 1
	s_mov_b32 s30, 0xff800000
	s_cmp_eq_u32 s27, 0
	s_cbranch_scc1 .Lk1_lse
	s_mov_b32 s37, 0x7fffffff
	v_cmp_eq_f32_e64 s[64:65], s28, v16
	v_cmp_eq_f32_e64 s[66:67], s28, v17
	v_cmp_eq_f32_e64 s[68:69], s28, v18
	v_cmp_eq_f32_e64 s[70:71], s28, v19
	s_or_b64 s[32:33], s[64:65], s[66:67]
	s_or_b64 s[72:73], s[68:69], s[70:71]
	s_or_b64 s[32:33], s[32:33], s[72:73]
	s_cmp_eq_u64 s[32:33], 0
	s_cbranch_scc1 .Lk1_a1_n0
	s_ff1_i32_b64 s32, s[64:65]
	s_lshl_b32 s33, s32, 2
	s_cmp_lt_i32 s32, 0
	s_cselect_b32 s33, 0x7fffffff, s33
	s_min_u32 s37, s37, s33
	s_ff1_i32_b64 s32, s[66:67]
	s_lshl_b32 s33, s32, 2
	s_add_u32 s33, s33, 1
	s_cmp_lt_i32 s32, 0
	s_cselect_b32 s33, 0x7fffffff, s33
	s_min_u32 s37, s37, s33
	s_ff1_i32_b64 s32, s[68:69]
	s_lshl_b32 s33, s32, 2
	s_add_u32 s33, s33, 2
	s_cmp_lt_i32 s32, 0
	s_cselect_b32 s33, 0x7fffffff, s33
	s_min_u32 s37, s37, s33
	s_ff1_i32_b64 s32, s[70:71]
	s_lshl_b32 s33, s32, 2
	s_add_u32 s33, s33, 3
	s_cmp_lt_i32 s32, 0
	s_cselect_b32 s33, 0x7fffffff, s33
	s_min_u32 s37, s37, s33
	s_lshr_b32 s32, s37, 2
	s_and_b32 s33, s37, 3
	s_lshl_b64 s[72:73], 1, s32
	s_cmp_eq_u32 s33, 0
	s_cselect_b64 s[64:65], s[72:73], 0
	v_cndmask_b32_e64 v16, v16, v15, s[64:65]
	s_cmp_eq_u32 s33, 1
	s_cselect_b64 s[64:65], s[72:73], 0
	v_cndmask_b32_e64 v17, v17, v15, s[64:65]
	s_cmp_eq_u32 s33, 2
	s_cselect_b64 s[64:65], s[72:73], 0
	v_cndmask_b32_e64 v18, v18, v15, s[64:65]
	s_cmp_eq_u32 s33, 3
	s_cselect_b64 s[64:65], s[72:73], 0
	v_cndmask_b32_e64 v19, v19, v15, s[64:65]
	s_sub_u32 s37, s37, s35
	s_branch .Lk1_a1_done
